# speedup vs baseline: 1.0181x; 1.0181x over previous
.LBB2_32:
	s_or_b64 exec, exec, s[34:35]
	s_waitcnt lgkmcnt(0)
	s_barrier
	v_lshlrev_b32_e32 v10, 2, v0
	v_readfirstlane_b32 s3, v17
	s_cmp_gt_u32 s3, 7
	s_cbranch_scc1 .Lmf_skip
	v_and_b32_e32 v2, 15, v1
	v_lshrrev_b32_e32 v3, 4, v1
	v_mul_u32_u24_e32 v5, 0x410, v2
	v_lshl_add_u32 v5, v3, 5, v5
	s_lshl_b32 s8, s3, 7
	s_lshl_b32 s9, s3, 9
	s_add_u32 s9, s9, 0x5140
	v_add_u32_e32 v5, s8, v5
	ds_read_b128 v[18:21], v5
	ds_read_b128 v[26:29], v5 offset:10400
	ds_read_b128 v[22:25], v5 offset:16
	ds_read_b128 v[30:33], v5 offset:10416
	v_mul_u32_u24_e32 v11, 0xa0, v3
	v_lshl_add_u32 v11, v2, 2, v11
	v_add_u32_e32 v11, s9, v11
	v_cmp_gt_u32_e64 s[10:11], 10, v2
	v_cmp_gt_u32_e64 s[12:13], 3, v3
	v_cmp_gt_u32_e64 s[14:15], 2, v3
	s_and_b64 s[12:13], s[10:11], s[12:13]
	s_and_b64 s[14:15], s[10:11], s[14:15]
	s_waitcnt lgkmcnt(3)
	v_mfma_f32_16x16x4_f32 v[34:37], v18, v18, 0
	s_waitcnt lgkmcnt(2)
	v_mfma_f32_16x16x4_f32 v[38:41], v26, v26, 0
	v_mfma_f32_16x16x4_f32 v[34:37], v19, v19, v[34:37]
	v_mfma_f32_16x16x4_f32 v[38:41], v27, v27, v[38:41]
	v_mfma_f32_16x16x4_f32 v[34:37], v20, v20, v[34:37]
	v_mfma_f32_16x16x4_f32 v[38:41], v28, v28, v[38:41]
	v_mfma_f32_16x16x4_f32 v[34:37], v21, v21, v[34:37]
	v_mfma_f32_16x16x4_f32 v[38:41], v29, v29, v[38:41]
	s_waitcnt lgkmcnt(0)
	v_mfma_f32_16x16x4_f32 v[34:37], v22, v22, v[34:37]
	v_mfma_f32_16x16x4_f32 v[38:41], v30, v30, v[38:41]
	v_mfma_f32_16x16x4_f32 v[34:37], v23, v23, v[34:37]
	v_mfma_f32_16x16x4_f32 v[38:41], v31, v31, v[38:41]
	v_mfma_f32_16x16x4_f32 v[34:37], v24, v24, v[34:37]
	v_mfma_f32_16x16x4_f32 v[38:41], v32, v32, v[38:41]
	v_mfma_f32_16x16x4_f32 v[34:37], v25, v25, v[34:37]
	v_mfma_f32_16x16x4_f32 v[38:41], v33, v33, v[38:41]
	s_nop 11
	s_mov_b64 s[6:7], exec
	s_mov_b64 exec, s[12:13]
	ds_write_b32 v11, v34
	ds_write_b32 v11, v35 offset:40
	ds_write_b32 v11, v38 offset:4096
	ds_write_b32 v11, v39 offset:4136
	s_mov_b64 exec, s[14:15]
	ds_write_b32 v11, v36 offset:80
	ds_write_b32 v11, v37 offset:120
	ds_write_b32 v11, v40 offset:4176
	ds_write_b32 v11, v41 offset:4216
	s_mov_b64 exec, s[6:7]
.Lmf_skip:
	s_movk_i32 s3, 0x80
	v_cmp_gt_u32_e32 vcc, s3, v0
	s_waitcnt lgkmcnt(0)
	s_barrier
	s_and_saveexec_b64 s[6:7], vcc
	s_cbranch_execz .LBB2_34
	v_add_u32_e32 v5, 64, v10
	ds_read2st64_b32 v[2:3], v5 offset0:81 offset1:83
	ds_read2st64_b32 v[12:13], v5 offset0:97 offset1:99
	ds_read2st64_b32 v[14:15], v5 offset0:85 offset1:87
	ds_read2st64_b32 v[18:19], v5 offset0:101 offset1:103
	s_waitcnt lgkmcnt(3)
	v_add_f32_e32 v2, 0, v2
	v_add_f32_e32 v2, v2, v3
	s_waitcnt lgkmcnt(2)
	v_add_f32_e32 v11, 0, v12
	s_waitcnt lgkmcnt(1)
	v_add_f32_e32 v12, v2, v14
	ds_read2st64_b32 v[2:3], v5 offset0:89 offset1:91
	v_add_f32_e32 v11, v11, v13
	v_add_f32_e32 v14, v12, v15
	ds_read2st64_b32 v[12:13], v5 offset0:105 offset1:107
	s_waitcnt lgkmcnt(2)
	v_add_f32_e32 v11, v11, v18
	v_add_f32_e32 v11, v11, v19
	s_waitcnt lgkmcnt(1)
	v_add_f32_e32 v2, v14, v2
	ds_read2st64_b32 v[14:15], v5 offset0:93 offset1:95
	ds_read2st64_b32 v[18:19], v5 offset0:109 offset1:111
	s_waitcnt lgkmcnt(2)
	v_add_f32_e32 v11, v11, v12
	v_add_f32_e32 v2, v2, v3
	v_add_f32_e32 v3, v11, v13
	s_waitcnt lgkmcnt(1)
	v_add_f32_e32 v2, v2, v14
	s_waitcnt lgkmcnt(0)
	v_add_f32_e32 v3, v3, v18
	v_add_f32_e32 v2, v2, v15
	v_add_f32_e32 v3, v3, v19
	ds_write2st64_b32 v5, v2, v3 offset0:116 offset1:118
